# G1 rope epilogue: cos/sin table loads software-pipelined 4 row groups deep (no per-row-group vmcnt(0) store drain)
# speedup vs baseline: 1.0287x; 1.0004x over previous
.LBB0_321:
	s_andn2_b64 vcc, exec, s[26:27]
	s_cbranch_vccnz .LBB0_323
	s_branch .Lg1rope_fast
	s_cselect_b64 vcc, -1, 0
	s_movk_i32 s3, 0x40ff
	v_cndmask_b32_e32 v134, 1.0, v202, vcc
	v_ashrrev_i32_e32 v133, 31, v64
	v_mov_b32_e32 v132, v64
	v_mov_b64_e32 v[130:131], s[8:9]
	s_movk_i32 s19, 0x2400
	v_cmp_lt_i32_e32 vcc, s3, v189
	v_add_u32_e32 v135, 0xffffbf00, v189
	v_mad_i64_i32 v[136:137], s[24:25], v189, s19, v[130:131]
	v_lshlrev_b64 v[132:133], 1, v[132:133]
	v_cndmask_b32_e32 v135, v189, v135, vcc
	v_lshl_add_u64 v[144:145], v[136:137], 0, v[132:133]
	s_movk_i32 s17, 0xff
	v_add_u32_e32 v136, 0xffffff00, v135
	v_cmp_lt_i32_e32 vcc, s17, v135
	v_lshrrev_b32_e32 v136, 6, v136
	v_and_b32_e32 v135, 15, v135
	v_cndmask_b32_e64 v135, v135, v136, s[4:5]
	v_lshlrev_b32_e32 v135, 6, v135
	v_cndmask_b32_e32 v135, 0, v135, vcc
	v_or_b32_e32 v136, v135, v187
	v_mov_b32_e32 v137, v65
	v_lshl_add_u64 v[140:141], v[136:137], 2, s[12:13]
	global_load_dwordx4 v[136:139], v[140:141], off offset:16
	s_nop 0
	global_load_dwordx4 v[140:143], v[140:141], off
	v_pk_mul_f32 v[160:161], v[134:135], v[126:127] op_sel_hi:[0,1]
	v_pk_mul_f32 v[158:159], v[134:135], v[128:129] op_sel_hi:[0,1]
	v_pk_mul_f32 v[162:163], v[134:135], v[124:125] op_sel_hi:[0,1]
	v_pk_mul_f32 v[164:165], v[134:135], v[122:123] op_sel_hi:[0,1]
	s_waitcnt vmcnt(0)
	v_pk_mul_f32 v[166:167], v[160:161], v[140:141]
	v_pk_mul_f32 v[160:161], v[160:161], v[140:141] op_sel:[0,1] op_sel_hi:[1,0]
	v_sub_f32_e32 v135, v166, v167
	v_add_f32_e32 v166, v160, v161
	v_pk_mul_f32 v[160:161], v[158:159], v[142:143]
	v_pk_mul_f32 v[158:159], v[158:159], v[142:143] op_sel:[0,1] op_sel_hi:[1,0]
	v_sub_f32_e32 v160, v160, v161
	v_add_f32_e32 v161, v158, v159
	v_pk_mul_f32 v[158:159], v[164:165], v[136:137]
	s_nop 0
	v_sub_f32_e32 v167, v158, v159
	v_pk_mul_f32 v[158:159], v[164:165], v[136:137] op_sel:[0,1] op_sel_hi:[1,0]
	s_nop 0
	v_add_f32_e32 v164, v158, v159
	v_pk_mul_f32 v[158:159], v[162:163], v[138:139]
	s_nop 0
	v_sub_f32_e32 v165, v158, v159
	v_pk_mul_f32 v[158:159], v[162:163], v[138:139] op_sel:[0,1] op_sel_hi:[1,0]
	s_nop 0
	v_add_f32_e32 v162, v158, v159
	v_cvt_pk_bf16_f32 v158, v135, v166
	v_cvt_pk_bf16_f32 v159, v160, v161
	v_cvt_pk_bf16_f32 v160, v167, v164
	v_cvt_pk_bf16_f32 v161, v165, v162
	global_store_dwordx4 v[144:145], v[158:161], off
	v_pk_mul_f32 v[164:165], v[134:135], v[106:107] op_sel_hi:[0,1]
	v_pk_mul_f32 v[162:163], v[134:135], v[108:109] op_sel_hi:[0,1]
	v_pk_mul_f32 v[160:161], v[134:135], v[114:115] op_sel_hi:[0,1]
	v_pk_mul_f32 v[158:159], v[134:135], v[116:117] op_sel_hi:[0,1]
	v_pk_mul_f32 v[166:167], v[160:161], v[140:141]
	v_pk_mul_f32 v[140:141], v[160:161], v[140:141] op_sel:[0,1] op_sel_hi:[1,0]
	v_sub_f32_e32 v135, v166, v167
	v_add_f32_e32 v160, v140, v141
	v_pk_mul_f32 v[140:141], v[158:159], v[142:143]
	s_nop 0
	v_sub_f32_e32 v161, v140, v141
	v_pk_mul_f32 v[140:141], v[158:159], v[142:143] op_sel:[0,1] op_sel_hi:[1,0]
	s_nop 0
	v_add_f32_e32 v142, v140, v141
	v_pk_mul_f32 v[140:141], v[164:165], v[136:137]
	v_pk_mul_f32 v[136:137], v[164:165], v[136:137] op_sel:[0,1] op_sel_hi:[1,0]
	v_sub_f32_e32 v140, v140, v141
	v_add_f32_e32 v141, v136, v137
	v_pk_mul_f32 v[136:137], v[162:163], v[138:139]
	s_nop 0
	v_sub_f32_e32 v143, v136, v137
	v_pk_mul_f32 v[136:137], v[162:163], v[138:139] op_sel:[0,1] op_sel_hi:[1,0]
	s_nop 0
	v_add_f32_e32 v139, v136, v137
	v_cvt_pk_bf16_f32 v136, v135, v160
	v_cvt_pk_bf16_f32 v137, v161, v142
	v_cvt_pk_bf16_f32 v138, v140, v141
	v_or_b32_e32 v135, 16, v189
	v_cvt_pk_bf16_f32 v139, v143, v139
	global_store_dwordx4 v[144:145], v[136:139], off offset:256
	v_cmp_lt_i32_e32 vcc, s3, v135
	s_nop 0
	v_add_u32_e32 v138, 0xffffbf10, v189
	v_mad_i64_i32 v[136:137], s[24:25], v135, s19, v[130:131]
	v_cndmask_b32_e32 v135, v135, v138, vcc
	v_add_u32_e32 v138, 0xffffff00, v135
	v_cmp_lt_i32_e32 vcc, s17, v135
	v_lshrrev_b32_e32 v138, 6, v138
	v_and_b32_e32 v135, 31, v135
	v_cndmask_b32_e64 v135, v135, v138, s[4:5]
	v_lshlrev_b32_e32 v135, 6, v135
	v_cndmask_b32_e32 v135, 0, v135, vcc
	v_or_b32_e32 v138, v135, v187
	v_mov_b32_e32 v139, v65
	v_lshl_add_u64 v[142:143], v[138:139], 2, s[12:13]
	global_load_dwordx4 v[138:141], v[142:143], off offset:16
	s_nop 0
	global_load_dwordx4 v[142:145], v[142:143], off
	v_pk_mul_f32 v[160:161], v[134:135], v[118:119] op_sel_hi:[0,1]
	v_pk_mul_f32 v[158:159], v[134:135], v[120:121] op_sel_hi:[0,1]
	v_pk_mul_f32 v[162:163], v[134:135], v[112:113] op_sel_hi:[0,1]
	v_pk_mul_f32 v[164:165], v[134:135], v[110:111] op_sel_hi:[0,1]
	v_lshl_add_u64 v[136:137], v[136:137], 0, v[132:133]
	s_waitcnt vmcnt(0)
	v_pk_mul_f32 v[166:167], v[160:161], v[142:143]
	v_pk_mul_f32 v[160:161], v[160:161], v[142:143] op_sel:[0,1] op_sel_hi:[1,0]
	v_sub_f32_e32 v135, v166, v167
	v_add_f32_e32 v166, v160, v161
	v_pk_mul_f32 v[160:161], v[158:159], v[144:145]
	v_pk_mul_f32 v[158:159], v[158:159], v[144:145] op_sel:[0,1] op_sel_hi:[1,0]
	v_sub_f32_e32 v160, v160, v161
	v_add_f32_e32 v161, v158, v159
	v_pk_mul_f32 v[158:159], v[164:165], v[138:139]
	s_nop 0
	v_sub_f32_e32 v167, v158, v159
	v_pk_mul_f32 v[158:159], v[164:165], v[138:139] op_sel:[0,1] op_sel_hi:[1,0]
	s_nop 0
	v_add_f32_e32 v164, v158, v159
	v_pk_mul_f32 v[158:159], v[162:163], v[140:141]
	s_nop 0
	v_sub_f32_e32 v165, v158, v159
	v_pk_mul_f32 v[158:159], v[162:163], v[140:141] op_sel:[0,1] op_sel_hi:[1,0]
	s_nop 0
	v_add_f32_e32 v162, v158, v159
	v_cvt_pk_bf16_f32 v158, v135, v166
	v_cvt_pk_bf16_f32 v159, v160, v161
	v_cvt_pk_bf16_f32 v160, v167, v164
	v_cvt_pk_bf16_f32 v161, v165, v162
	global_store_dwordx4 v[136:137], v[158:161], off
	v_pk_mul_f32 v[164:165], v[134:135], v[90:91] op_sel_hi:[0,1]
	v_pk_mul_f32 v[162:163], v[134:135], v[92:93] op_sel_hi:[0,1]
	v_pk_mul_f32 v[160:161], v[134:135], v[98:99] op_sel_hi:[0,1]
	v_pk_mul_f32 v[158:159], v[134:135], v[100:101] op_sel_hi:[0,1]
	v_pk_mul_f32 v[166:167], v[160:161], v[142:143]
	v_pk_mul_f32 v[142:143], v[160:161], v[142:143] op_sel:[0,1] op_sel_hi:[1,0]
	v_sub_f32_e32 v135, v166, v167
	v_add_f32_e32 v160, v142, v143
	v_pk_mul_f32 v[142:143], v[158:159], v[144:145]
	s_nop 0
	v_sub_f32_e32 v161, v142, v143
	v_pk_mul_f32 v[142:143], v[158:159], v[144:145] op_sel:[0,1] op_sel_hi:[1,0]
	s_nop 0
	v_add_f32_e32 v144, v142, v143
	v_pk_mul_f32 v[142:143], v[164:165], v[138:139]
	v_pk_mul_f32 v[138:139], v[164:165], v[138:139] op_sel:[0,1] op_sel_hi:[1,0]
	v_sub_f32_e32 v142, v142, v143
	v_add_f32_e32 v143, v138, v139
	v_pk_mul_f32 v[138:139], v[162:163], v[140:141]
	s_nop 0
	v_sub_f32_e32 v145, v138, v139
	v_pk_mul_f32 v[138:139], v[162:163], v[140:141] op_sel:[0,1] op_sel_hi:[1,0]
	s_nop 0
	v_add_f32_e32 v141, v138, v139
	v_cvt_pk_bf16_f32 v138, v135, v160
	v_or_b32_e32 v135, 32, v189
	v_cvt_pk_bf16_f32 v139, v161, v144
	v_cvt_pk_bf16_f32 v140, v142, v143
	v_cvt_pk_bf16_f32 v141, v145, v141
	global_store_dwordx4 v[136:137], v[138:141], off offset:256
	v_cmp_lt_i32_e32 vcc, s3, v135
	v_mad_i64_i32 v[136:137], s[24:25], v135, s19, v[130:131]
	v_add_u32_e32 v138, 0xffffbf20, v189
	v_cndmask_b32_e32 v135, v135, v138, vcc
	v_add_u32_e32 v138, 0xffffff00, v135
	v_cmp_lt_i32_e32 vcc, s17, v135
	v_lshrrev_b32_e32 v138, 6, v138
	v_and_b32_e32 v135, 47, v135
	v_cndmask_b32_e64 v135, v135, v138, s[4:5]
	v_lshlrev_b32_e32 v135, 6, v135
	v_cndmask_b32_e32 v135, 0, v135, vcc
	v_or_b32_e32 v138, v135, v187
	v_mov_b32_e32 v139, v65
	v_lshl_add_u64 v[142:143], v[138:139], 2, s[12:13]
	global_load_dwordx4 v[138:141], v[142:143], off offset:16
	s_nop 0
	global_load_dwordx4 v[142:145], v[142:143], off
	v_pk_mul_f32 v[160:161], v[134:135], v[102:103] op_sel_hi:[0,1]
	v_pk_mul_f32 v[158:159], v[134:135], v[104:105] op_sel_hi:[0,1]
	v_pk_mul_f32 v[162:163], v[134:135], v[96:97] op_sel_hi:[0,1]
	v_pk_mul_f32 v[164:165], v[134:135], v[94:95] op_sel_hi:[0,1]
	v_lshl_add_u64 v[136:137], v[136:137], 0, v[132:133]
	s_waitcnt vmcnt(0)
	v_pk_mul_f32 v[166:167], v[160:161], v[142:143]
	v_pk_mul_f32 v[160:161], v[160:161], v[142:143] op_sel:[0,1] op_sel_hi:[1,0]
	v_sub_f32_e32 v135, v166, v167
	v_add_f32_e32 v166, v160, v161
	v_pk_mul_f32 v[160:161], v[158:159], v[144:145]
	v_pk_mul_f32 v[158:159], v[158:159], v[144:145] op_sel:[0,1] op_sel_hi:[1,0]
	v_sub_f32_e32 v160, v160, v161
	v_add_f32_e32 v161, v158, v159
	v_pk_mul_f32 v[158:159], v[164:165], v[138:139]
	s_nop 0
	v_sub_f32_e32 v167, v158, v159
	v_pk_mul_f32 v[158:159], v[164:165], v[138:139] op_sel:[0,1] op_sel_hi:[1,0]
	s_nop 0
	v_add_f32_e32 v164, v158, v159
	v_pk_mul_f32 v[158:159], v[162:163], v[140:141]
	s_nop 0
	v_sub_f32_e32 v165, v158, v159
	v_pk_mul_f32 v[158:159], v[162:163], v[140:141] op_sel:[0,1] op_sel_hi:[1,0]
	s_nop 0
	v_add_f32_e32 v162, v158, v159
	v_cvt_pk_bf16_f32 v158, v135, v166
	v_cvt_pk_bf16_f32 v159, v160, v161
	v_cvt_pk_bf16_f32 v160, v167, v164
	v_cvt_pk_bf16_f32 v161, v165, v162
	global_store_dwordx4 v[136:137], v[158:161], off
	v_pk_mul_f32 v[164:165], v[134:135], v[74:75] op_sel_hi:[0,1]
	v_pk_mul_f32 v[162:163], v[134:135], v[76:77] op_sel_hi:[0,1]
	v_pk_mul_f32 v[160:161], v[134:135], v[82:83] op_sel_hi:[0,1]
	v_pk_mul_f32 v[158:159], v[134:135], v[84:85] op_sel_hi:[0,1]
	v_pk_mul_f32 v[166:167], v[160:161], v[142:143]
	v_pk_mul_f32 v[142:143], v[160:161], v[142:143] op_sel:[0,1] op_sel_hi:[1,0]
	v_sub_f32_e32 v135, v166, v167
	v_add_f32_e32 v160, v142, v143
	v_pk_mul_f32 v[142:143], v[158:159], v[144:145]
	s_nop 0
	v_sub_f32_e32 v161, v142, v143
	v_pk_mul_f32 v[142:143], v[158:159], v[144:145] op_sel:[0,1] op_sel_hi:[1,0]
	s_nop 0
	v_add_f32_e32 v144, v142, v143
	v_pk_mul_f32 v[142:143], v[164:165], v[138:139]
	v_pk_mul_f32 v[138:139], v[164:165], v[138:139] op_sel:[0,1] op_sel_hi:[1,0]
	v_sub_f32_e32 v142, v142, v143
	v_add_f32_e32 v143, v138, v139
	v_pk_mul_f32 v[138:139], v[162:163], v[140:141]
	s_nop 0
	v_sub_f32_e32 v145, v138, v139
	v_pk_mul_f32 v[138:139], v[162:163], v[140:141] op_sel:[0,1] op_sel_hi:[1,0]
	s_nop 0
	v_add_f32_e32 v141, v138, v139
	v_cvt_pk_bf16_f32 v138, v135, v160
	v_or_b32_e32 v135, 48, v189
	v_cvt_pk_bf16_f32 v139, v161, v144
	v_cvt_pk_bf16_f32 v140, v142, v143
	v_cvt_pk_bf16_f32 v141, v145, v141
	global_store_dwordx4 v[136:137], v[138:141], off offset:256
	v_cmp_lt_i32_e32 vcc, s3, v135
	v_mad_i64_i32 v[136:137], s[24:25], v135, s19, v[130:131]
	v_add_u32_e32 v138, 0xffffbf30, v189
	v_cndmask_b32_e32 v135, v135, v138, vcc
	v_add_u32_e32 v138, 0xffffff00, v135
	v_cmp_lt_i32_e32 vcc, s17, v135
	v_lshrrev_b32_e32 v138, 6, v138
	v_and_b32_e32 v135, 63, v135
	v_cndmask_b32_e64 v135, v135, v138, s[4:5]
	v_lshlrev_b32_e32 v135, 6, v135
	v_cndmask_b32_e32 v135, 0, v135, vcc
	v_or_b32_e32 v138, v135, v187
	v_mov_b32_e32 v139, v65
	v_lshl_add_u64 v[142:143], v[138:139], 2, s[12:13]
	global_load_dwordx4 v[138:141], v[142:143], off offset:16
	s_nop 0
	global_load_dwordx4 v[142:145], v[142:143], off
	v_pk_mul_f32 v[160:161], v[134:135], v[86:87] op_sel_hi:[0,1]
	v_pk_mul_f32 v[158:159], v[134:135], v[88:89] op_sel_hi:[0,1]
	v_pk_mul_f32 v[162:163], v[134:135], v[80:81] op_sel_hi:[0,1]
	v_pk_mul_f32 v[164:165], v[134:135], v[78:79] op_sel_hi:[0,1]
	v_lshl_add_u64 v[136:137], v[136:137], 0, v[132:133]
	s_movk_i32 s3, 0x407f
	v_cmp_lt_i32_e32 vcc, s3, v189
	s_movk_i32 s3, 0x406f
	s_waitcnt vmcnt(0)
	v_pk_mul_f32 v[166:167], v[160:161], v[142:143]
	v_pk_mul_f32 v[160:161], v[160:161], v[142:143] op_sel:[0,1] op_sel_hi:[1,0]
	v_sub_f32_e32 v135, v166, v167
	v_add_f32_e32 v166, v160, v161
	v_pk_mul_f32 v[160:161], v[158:159], v[144:145]
	v_pk_mul_f32 v[158:159], v[158:159], v[144:145] op_sel:[0,1] op_sel_hi:[1,0]
	v_sub_f32_e32 v160, v160, v161
	v_add_f32_e32 v161, v158, v159
	v_pk_mul_f32 v[158:159], v[164:165], v[138:139]
	s_nop 0
	v_sub_f32_e32 v167, v158, v159
	v_pk_mul_f32 v[158:159], v[164:165], v[138:139] op_sel:[0,1] op_sel_hi:[1,0]
	s_nop 0
	v_add_f32_e32 v164, v158, v159
	v_pk_mul_f32 v[158:159], v[162:163], v[140:141]
	s_nop 0
	v_sub_f32_e32 v165, v158, v159
	v_pk_mul_f32 v[158:159], v[162:163], v[140:141] op_sel:[0,1] op_sel_hi:[1,0]
	s_nop 0
	v_add_f32_e32 v162, v158, v159
	v_cvt_pk_bf16_f32 v158, v135, v166
	v_cvt_pk_bf16_f32 v159, v160, v161
	v_cvt_pk_bf16_f32 v160, v167, v164
	v_cvt_pk_bf16_f32 v161, v165, v162
	global_store_dwordx4 v[136:137], v[158:161], off
	v_pk_mul_f32 v[164:165], v[134:135], v[66:67] op_sel_hi:[0,1]
	v_pk_mul_f32 v[162:163], v[134:135], v[68:69] op_sel_hi:[0,1]
	v_pk_mul_f32 v[160:161], v[134:135], v[70:71] op_sel_hi:[0,1]
	v_pk_mul_f32 v[158:159], v[134:135], v[72:73] op_sel_hi:[0,1]
	v_pk_mul_f32 v[166:167], v[160:161], v[142:143]
	v_pk_mul_f32 v[142:143], v[160:161], v[142:143] op_sel:[0,1] op_sel_hi:[1,0]
	v_sub_f32_e32 v135, v166, v167
	v_add_f32_e32 v160, v142, v143
	v_pk_mul_f32 v[142:143], v[158:159], v[144:145]
	s_nop 0
	v_sub_f32_e32 v161, v142, v143
	v_pk_mul_f32 v[142:143], v[158:159], v[144:145] op_sel:[0,1] op_sel_hi:[1,0]
	s_nop 0
	v_add_f32_e32 v144, v142, v143
	v_pk_mul_f32 v[142:143], v[164:165], v[138:139]
	v_pk_mul_f32 v[138:139], v[164:165], v[138:139] op_sel:[0,1] op_sel_hi:[1,0]
	v_sub_f32_e32 v142, v142, v143
	v_add_f32_e32 v143, v138, v139
	v_pk_mul_f32 v[138:139], v[162:163], v[140:141]
	s_nop 0
	v_sub_f32_e32 v145, v138, v139
	v_pk_mul_f32 v[138:139], v[162:163], v[140:141] op_sel:[0,1] op_sel_hi:[1,0]
	s_nop 0
	v_add_f32_e32 v141, v138, v139
	v_cvt_pk_bf16_f32 v138, v135, v160
	v_cvt_pk_bf16_f32 v139, v161, v144
	v_cvt_pk_bf16_f32 v140, v142, v143
	v_cvt_pk_bf16_f32 v141, v145, v141
	global_store_dwordx4 v[136:137], v[138:141], off offset:256
	v_add_u32_e32 v135, 0x80, v189
	v_mad_i64_i32 v[136:137], s[24:25], v135, s19, v[130:131]
	v_add_u32_e32 v138, 0xffffbf80, v189
	v_cndmask_b32_e32 v135, v135, v138, vcc
	v_add_u32_e32 v138, 0xffffff00, v135
	v_cmp_lt_i32_e32 vcc, s17, v135
	v_lshrrev_b32_e32 v138, 6, v138
	v_and_b32_e32 v135, 15, v135
	v_cndmask_b32_e64 v135, v135, v138, s[4:5]
	v_lshlrev_b32_e32 v135, 6, v135
	v_cndmask_b32_e32 v135, 0, v135, vcc
	v_or_b32_e32 v138, v135, v187
	v_mov_b32_e32 v139, v65
	v_lshl_add_u64 v[142:143], v[138:139], 2, s[12:13]
	global_load_dwordx4 v[138:141], v[142:143], off offset:16
	s_nop 0
	global_load_dwordx4 v[142:145], v[142:143], off
	v_pk_mul_f32 v[160:161], v[134:135], v[60:61] op_sel_hi:[0,1]
	v_pk_mul_f32 v[158:159], v[134:135], v[62:63] op_sel_hi:[0,1]
	v_pk_mul_f32 v[162:163], v[134:135], v[58:59] op_sel_hi:[0,1]
	v_pk_mul_f32 v[164:165], v[134:135], v[56:57] op_sel_hi:[0,1]
	v_lshl_add_u64 v[136:137], v[136:137], 0, v[132:133]
	v_cmp_lt_i32_e32 vcc, s3, v189
	s_movk_i32 s3, 0x405f
	s_waitcnt vmcnt(0)
	v_pk_mul_f32 v[166:167], v[160:161], v[142:143]
	v_pk_mul_f32 v[160:161], v[160:161], v[142:143] op_sel:[0,1] op_sel_hi:[1,0]
	v_sub_f32_e32 v135, v166, v167
	v_add_f32_e32 v166, v160, v161
	v_pk_mul_f32 v[160:161], v[158:159], v[144:145]
	v_pk_mul_f32 v[158:159], v[158:159], v[144:145] op_sel:[0,1] op_sel_hi:[1,0]
	v_sub_f32_e32 v160, v160, v161
	v_add_f32_e32 v161, v158, v159
	v_pk_mul_f32 v[158:159], v[164:165], v[138:139]
	s_nop 0
	v_sub_f32_e32 v167, v158, v159
	v_pk_mul_f32 v[158:159], v[164:165], v[138:139] op_sel:[0,1] op_sel_hi:[1,0]
	s_nop 0
	v_add_f32_e32 v164, v158, v159
	v_pk_mul_f32 v[158:159], v[162:163], v[140:141]
	s_nop 0
	v_sub_f32_e32 v165, v158, v159
	v_pk_mul_f32 v[158:159], v[162:163], v[140:141] op_sel:[0,1] op_sel_hi:[1,0]
	s_nop 0
	v_add_f32_e32 v162, v158, v159
	v_cvt_pk_bf16_f32 v158, v135, v166
	v_cvt_pk_bf16_f32 v159, v160, v161
	v_cvt_pk_bf16_f32 v160, v167, v164
	v_cvt_pk_bf16_f32 v161, v165, v162
	global_store_dwordx4 v[136:137], v[158:161], off
	v_pk_mul_f32 v[164:165], v[134:135], v[40:41] op_sel_hi:[0,1]
	v_pk_mul_f32 v[162:163], v[134:135], v[42:43] op_sel_hi:[0,1]
	v_pk_mul_f32 v[160:161], v[134:135], v[48:49] op_sel_hi:[0,1]
	v_pk_mul_f32 v[158:159], v[134:135], v[50:51] op_sel_hi:[0,1]
	v_pk_mul_f32 v[166:167], v[160:161], v[142:143]
	v_pk_mul_f32 v[142:143], v[160:161], v[142:143] op_sel:[0,1] op_sel_hi:[1,0]
	v_sub_f32_e32 v135, v166, v167
	v_add_f32_e32 v160, v142, v143
	v_pk_mul_f32 v[142:143], v[158:159], v[144:145]
	s_nop 0
	v_sub_f32_e32 v161, v142, v143
	v_pk_mul_f32 v[142:143], v[158:159], v[144:145] op_sel:[0,1] op_sel_hi:[1,0]
	s_nop 0
	v_add_f32_e32 v144, v142, v143
	v_pk_mul_f32 v[142:143], v[164:165], v[138:139]
	v_pk_mul_f32 v[138:139], v[164:165], v[138:139] op_sel:[0,1] op_sel_hi:[1,0]
	v_sub_f32_e32 v142, v142, v143
	v_add_f32_e32 v143, v138, v139
	v_pk_mul_f32 v[138:139], v[162:163], v[140:141]
	s_nop 0
	v_sub_f32_e32 v145, v138, v139
	v_pk_mul_f32 v[138:139], v[162:163], v[140:141] op_sel:[0,1] op_sel_hi:[1,0]
	s_nop 0
	v_add_f32_e32 v141, v138, v139
	v_cvt_pk_bf16_f32 v138, v135, v160
	v_cvt_pk_bf16_f32 v139, v161, v144
	v_cvt_pk_bf16_f32 v140, v142, v143
	v_cvt_pk_bf16_f32 v141, v145, v141
	global_store_dwordx4 v[136:137], v[138:141], off offset:256
	v_add_u32_e32 v135, 0x90, v189
	v_mad_i64_i32 v[136:137], s[24:25], v135, s19, v[130:131]
	v_add_u32_e32 v138, 0xffffbf90, v189
	v_cndmask_b32_e32 v135, v135, v138, vcc
	v_add_u32_e32 v138, 0xffffff00, v135
	v_cmp_lt_i32_e32 vcc, s17, v135
	v_lshrrev_b32_e32 v138, 6, v138
	v_and_b32_e32 v135, 31, v135
	v_cndmask_b32_e64 v135, v135, v138, s[4:5]
	v_lshlrev_b32_e32 v135, 6, v135
	v_cndmask_b32_e32 v135, 0, v135, vcc
	v_or_b32_e32 v138, v135, v187
	v_mov_b32_e32 v139, v65
	v_lshl_add_u64 v[142:143], v[138:139], 2, s[12:13]
	global_load_dwordx4 v[138:141], v[142:143], off offset:16
	s_nop 0
	global_load_dwordx4 v[142:145], v[142:143], off
	v_pk_mul_f32 v[160:161], v[134:135], v[52:53] op_sel_hi:[0,1]
	v_pk_mul_f32 v[158:159], v[134:135], v[54:55] op_sel_hi:[0,1]
	v_pk_mul_f32 v[162:163], v[134:135], v[46:47] op_sel_hi:[0,1]
	v_pk_mul_f32 v[164:165], v[134:135], v[44:45] op_sel_hi:[0,1]
	v_lshl_add_u64 v[136:137], v[136:137], 0, v[132:133]
	v_cmp_lt_i32_e32 vcc, s3, v189
	s_movk_i32 s3, 0x404f
	s_waitcnt vmcnt(0)
	v_pk_mul_f32 v[166:167], v[160:161], v[142:143]
	v_pk_mul_f32 v[160:161], v[160:161], v[142:143] op_sel:[0,1] op_sel_hi:[1,0]
	v_sub_f32_e32 v135, v166, v167
	v_add_f32_e32 v166, v160, v161
	v_pk_mul_f32 v[160:161], v[158:159], v[144:145]
	v_pk_mul_f32 v[158:159], v[158:159], v[144:145] op_sel:[0,1] op_sel_hi:[1,0]
	v_sub_f32_e32 v160, v160, v161
	v_add_f32_e32 v161, v158, v159
	v_pk_mul_f32 v[158:159], v[164:165], v[138:139]
	s_nop 0
	v_sub_f32_e32 v167, v158, v159
	v_pk_mul_f32 v[158:159], v[164:165], v[138:139] op_sel:[0,1] op_sel_hi:[1,0]
	s_nop 0
	v_add_f32_e32 v164, v158, v159
	v_pk_mul_f32 v[158:159], v[162:163], v[140:141]
	s_nop 0
	v_sub_f32_e32 v165, v158, v159
	v_pk_mul_f32 v[158:159], v[162:163], v[140:141] op_sel:[0,1] op_sel_hi:[1,0]
	s_nop 0
	v_add_f32_e32 v162, v158, v159
	v_cvt_pk_bf16_f32 v158, v135, v166
	v_cvt_pk_bf16_f32 v159, v160, v161
	v_cvt_pk_bf16_f32 v160, v167, v164
	v_cvt_pk_bf16_f32 v161, v165, v162
	global_store_dwordx4 v[136:137], v[158:161], off
	v_pk_mul_f32 v[164:165], v[134:135], v[24:25] op_sel_hi:[0,1]
	v_pk_mul_f32 v[162:163], v[134:135], v[26:27] op_sel_hi:[0,1]
	v_pk_mul_f32 v[160:161], v[134:135], v[32:33] op_sel_hi:[0,1]
	v_pk_mul_f32 v[158:159], v[134:135], v[34:35] op_sel_hi:[0,1]
	v_pk_mul_f32 v[166:167], v[160:161], v[142:143]
	v_pk_mul_f32 v[142:143], v[160:161], v[142:143] op_sel:[0,1] op_sel_hi:[1,0]
	v_sub_f32_e32 v135, v166, v167
	v_add_f32_e32 v160, v142, v143
	v_pk_mul_f32 v[142:143], v[158:159], v[144:145]
	s_nop 0
	v_sub_f32_e32 v161, v142, v143
	v_pk_mul_f32 v[142:143], v[158:159], v[144:145] op_sel:[0,1] op_sel_hi:[1,0]
	s_nop 0
	v_add_f32_e32 v144, v142, v143
	v_pk_mul_f32 v[142:143], v[164:165], v[138:139]
	v_pk_mul_f32 v[138:139], v[164:165], v[138:139] op_sel:[0,1] op_sel_hi:[1,0]
	v_sub_f32_e32 v142, v142, v143
	v_add_f32_e32 v143, v138, v139
	v_pk_mul_f32 v[138:139], v[162:163], v[140:141]
	s_nop 0
	v_sub_f32_e32 v145, v138, v139
	v_pk_mul_f32 v[138:139], v[162:163], v[140:141] op_sel:[0,1] op_sel_hi:[1,0]
	s_nop 0
	v_add_f32_e32 v141, v138, v139
	v_cvt_pk_bf16_f32 v138, v135, v160
	v_cvt_pk_bf16_f32 v139, v161, v144
	v_cvt_pk_bf16_f32 v140, v142, v143
	v_cvt_pk_bf16_f32 v141, v145, v141
	global_store_dwordx4 v[136:137], v[138:141], off offset:256
	v_add_u32_e32 v135, 0xa0, v189
	v_mad_i64_i32 v[136:137], s[24:25], v135, s19, v[130:131]
	v_add_u32_e32 v138, 0xffffbfa0, v189
	v_cndmask_b32_e32 v135, v135, v138, vcc
	v_add_u32_e32 v138, 0xffffff00, v135
	v_cmp_lt_i32_e32 vcc, s17, v135
	v_lshrrev_b32_e32 v138, 6, v138
	v_and_b32_e32 v135, 47, v135
	v_cndmask_b32_e64 v135, v135, v138, s[4:5]
	v_lshlrev_b32_e32 v135, 6, v135
	v_cndmask_b32_e32 v135, 0, v135, vcc
	v_or_b32_e32 v138, v135, v187
	v_mov_b32_e32 v139, v65
	v_lshl_add_u64 v[142:143], v[138:139], 2, s[12:13]
	global_load_dwordx4 v[138:141], v[142:143], off offset:16
	s_nop 0
	global_load_dwordx4 v[142:145], v[142:143], off
	v_pk_mul_f32 v[160:161], v[134:135], v[36:37] op_sel_hi:[0,1]
	v_pk_mul_f32 v[158:159], v[134:135], v[38:39] op_sel_hi:[0,1]
	v_pk_mul_f32 v[162:163], v[134:135], v[30:31] op_sel_hi:[0,1]
	v_pk_mul_f32 v[164:165], v[134:135], v[28:29] op_sel_hi:[0,1]
	v_lshl_add_u64 v[136:137], v[136:137], 0, v[132:133]
	v_cmp_lt_i32_e32 vcc, s3, v189
	s_waitcnt vmcnt(0)
	v_pk_mul_f32 v[166:167], v[160:161], v[142:143]
	v_pk_mul_f32 v[160:161], v[160:161], v[142:143] op_sel:[0,1] op_sel_hi:[1,0]
	v_sub_f32_e32 v135, v166, v167
	v_add_f32_e32 v166, v160, v161
	v_pk_mul_f32 v[160:161], v[158:159], v[144:145]
	v_pk_mul_f32 v[158:159], v[158:159], v[144:145] op_sel:[0,1] op_sel_hi:[1,0]
	v_sub_f32_e32 v160, v160, v161
	v_add_f32_e32 v161, v158, v159
	v_pk_mul_f32 v[158:159], v[164:165], v[138:139]
	s_nop 0
	v_sub_f32_e32 v167, v158, v159
	v_pk_mul_f32 v[158:159], v[164:165], v[138:139] op_sel:[0,1] op_sel_hi:[1,0]
	s_nop 0
	v_add_f32_e32 v164, v158, v159
	v_pk_mul_f32 v[158:159], v[162:163], v[140:141]
	s_nop 0
	v_sub_f32_e32 v165, v158, v159
	v_pk_mul_f32 v[158:159], v[162:163], v[140:141] op_sel:[0,1] op_sel_hi:[1,0]
	s_nop 0
	v_add_f32_e32 v162, v158, v159
	v_cvt_pk_bf16_f32 v158, v135, v166
	v_cvt_pk_bf16_f32 v159, v160, v161
	v_cvt_pk_bf16_f32 v160, v167, v164
	v_cvt_pk_bf16_f32 v161, v165, v162
	global_store_dwordx4 v[136:137], v[158:161], off
	v_pk_mul_f32 v[164:165], v[134:135], v[8:9] op_sel_hi:[0,1]
	v_pk_mul_f32 v[162:163], v[134:135], v[10:11] op_sel_hi:[0,1]
	v_pk_mul_f32 v[160:161], v[134:135], v[16:17] op_sel_hi:[0,1]
	v_pk_mul_f32 v[158:159], v[134:135], v[18:19] op_sel_hi:[0,1]
	v_pk_mul_f32 v[166:167], v[160:161], v[142:143]
	v_pk_mul_f32 v[142:143], v[160:161], v[142:143] op_sel:[0,1] op_sel_hi:[1,0]
	v_sub_f32_e32 v135, v166, v167
	v_add_f32_e32 v160, v142, v143
	v_pk_mul_f32 v[142:143], v[158:159], v[144:145]
	s_nop 0
	v_sub_f32_e32 v161, v142, v143
	v_pk_mul_f32 v[142:143], v[158:159], v[144:145] op_sel:[0,1] op_sel_hi:[1,0]
	s_nop 0
	v_add_f32_e32 v144, v142, v143
	v_pk_mul_f32 v[142:143], v[164:165], v[138:139]
	v_pk_mul_f32 v[138:139], v[164:165], v[138:139] op_sel:[0,1] op_sel_hi:[1,0]
	v_sub_f32_e32 v142, v142, v143
	v_add_f32_e32 v143, v138, v139
	v_pk_mul_f32 v[138:139], v[162:163], v[140:141]
	s_nop 0
	v_sub_f32_e32 v145, v138, v139
	v_pk_mul_f32 v[138:139], v[162:163], v[140:141] op_sel:[0,1] op_sel_hi:[1,0]
	s_nop 0
	v_add_f32_e32 v141, v138, v139
	v_cvt_pk_bf16_f32 v138, v135, v160
	v_add_u32_e32 v135, 0xb0, v189
	v_mad_i64_i32 v[130:131], s[24:25], v135, s19, v[130:131]
	v_lshl_add_u64 v[162:163], v[130:131], 0, v[132:133]
	v_add_u32_e32 v130, 0xffffbfb0, v189
	v_cndmask_b32_e32 v130, v135, v130, vcc
	v_add_u32_e32 v131, 0xffffff00, v130
	v_cmp_lt_i32_e32 vcc, s17, v130
	v_lshrrev_b32_e32 v131, 6, v131
	v_and_b32_e32 v130, 63, v130
	v_cndmask_b32_e64 v130, v130, v131, s[4:5]
	v_lshlrev_b32_e32 v130, 6, v130
	v_cndmask_b32_e32 v130, 0, v130, vcc
	v_or_b32_e32 v130, v130, v187
	v_mov_b32_e32 v131, v65
	v_cvt_pk_bf16_f32 v139, v161, v144
	v_cvt_pk_bf16_f32 v140, v142, v143
	v_cvt_pk_bf16_f32 v141, v145, v141
	global_store_dwordx4 v[136:137], v[138:141], off offset:256
	v_lshl_add_u64 v[136:137], v[130:131], 2, s[12:13]
	global_load_dwordx4 v[130:133], v[136:137], off offset:16
	s_nop 0
	global_load_dwordx4 v[136:139], v[136:137], off
	v_pk_mul_f32 v[142:143], v[134:135], v[20:21] op_sel_hi:[0,1]
	v_pk_mul_f32 v[140:141], v[134:135], v[22:23] op_sel_hi:[0,1]
	v_pk_mul_f32 v[144:145], v[134:135], v[14:15] op_sel_hi:[0,1]
	v_pk_mul_f32 v[158:159], v[134:135], v[12:13] op_sel_hi:[0,1]
	s_waitcnt vmcnt(0)
	v_pk_mul_f32 v[160:161], v[142:143], v[136:137]
	v_pk_mul_f32 v[142:143], v[142:143], v[136:137] op_sel:[0,1] op_sel_hi:[1,0]
	v_sub_f32_e32 v135, v160, v161
	v_add_f32_e32 v160, v142, v143
	v_pk_mul_f32 v[142:143], v[140:141], v[138:139]
	v_pk_mul_f32 v[140:141], v[140:141], v[138:139] op_sel:[0,1] op_sel_hi:[1,0]
	v_sub_f32_e32 v142, v142, v143
	v_add_f32_e32 v143, v140, v141
	v_pk_mul_f32 v[140:141], v[158:159], v[130:131]
	s_nop 0
	v_sub_f32_e32 v161, v140, v141
	v_pk_mul_f32 v[140:141], v[158:159], v[130:131] op_sel:[0,1] op_sel_hi:[1,0]
	s_nop 0
	v_add_f32_e32 v158, v140, v141
	v_pk_mul_f32 v[140:141], v[144:145], v[132:133]
	s_nop 0
	v_sub_f32_e32 v159, v140, v141
	v_pk_mul_f32 v[140:141], v[144:145], v[132:133] op_sel:[0,1] op_sel_hi:[1,0]
	s_nop 0
	v_add_f32_e32 v144, v140, v141
	v_cvt_pk_bf16_f32 v140, v135, v160
	v_cvt_pk_bf16_f32 v141, v142, v143
	v_cvt_pk_bf16_f32 v142, v161, v158
	v_cvt_pk_bf16_f32 v143, v159, v144
	global_store_dwordx4 v[162:163], v[140:143], off
	v_pk_mul_f32 v[144:145], v[134:135], v[2:3] op_sel_hi:[0,1]
	s_nop 0
	v_pk_mul_f32 v[142:143], v[134:135], v[4:5] op_sel_hi:[0,1]
	v_pk_mul_f32 v[140:141], v[134:135], v[6:7] op_sel_hi:[0,1]
	v_pk_mul_f32 v[158:159], v[142:143], v[136:137]
	v_pk_mul_f32 v[136:137], v[142:143], v[136:137] op_sel:[0,1] op_sel_hi:[1,0]
	v_pk_mul_f32 v[134:135], v[134:135], v[0:1] op_sel_hi:[0,1]
	v_add_f32_e32 v142, v136, v137
	v_pk_mul_f32 v[136:137], v[140:141], v[138:139]
	v_sub_f32_e32 v158, v158, v159
	v_sub_f32_e32 v143, v136, v137
	v_pk_mul_f32 v[136:137], v[140:141], v[138:139] op_sel:[0,1] op_sel_hi:[1,0]
	s_nop 0
	v_add_f32_e32 v138, v136, v137
	v_pk_mul_f32 v[136:137], v[134:135], v[130:131]
	v_pk_mul_f32 v[130:131], v[134:135], v[130:131] op_sel:[0,1] op_sel_hi:[1,0]
	v_sub_f32_e32 v136, v136, v137
	v_add_f32_e32 v134, v130, v131
	v_pk_mul_f32 v[130:131], v[144:145], v[132:133]
	s_nop 0
	v_sub_f32_e32 v135, v130, v131
	v_pk_mul_f32 v[130:131], v[144:145], v[132:133] op_sel:[0,1] op_sel_hi:[1,0]
	s_nop 0
	v_add_f32_e32 v133, v130, v131
	v_cvt_pk_bf16_f32 v130, v158, v142
	v_cvt_pk_bf16_f32 v131, v143, v138
	v_cvt_pk_bf16_f32 v132, v136, v134
	v_cvt_pk_bf16_f32 v133, v135, v133
	s_cbranch_execz .LBB0_324
	s_branch .LBB0_325
.Lg1rope_fast:
	s_cmp_eq_u32 s2, 6
	s_cselect_b64 vcc, -1, 0
	s_movk_i32 s3, 0x40ff
	v_cndmask_b32_e32 v134, 1.0, v202, vcc
	v_ashrrev_i32_e32 v139, 31, v64
	v_mov_b32_e32 v138, v64
	v_mov_b64_e32 v[136:137], s[8:9]
	s_movk_i32 s19, 0x2400
	s_movk_i32 s17, 0xff
	v_lshlrev_b64 v[138:139], 1, v[138:139]
	v_mov_b32_e32 v158, v189
	v_cmp_lt_i32_e32 vcc, s3, v158
	v_add_u32_e32 v159, 0xffffbf00, v158
	s_nop 1
	v_cndmask_b32_e32 v158, v158, v159, vcc
	v_add_u32_e32 v159, 0xffffff00, v158
	v_cmp_lt_i32_e32 vcc, s17, v158
	v_lshrrev_b32_e32 v159, 6, v159
	v_and_b32_e32 v158, 63, v158
	v_cndmask_b32_e64 v158, v158, v159, s[4:5]
	v_lshlrev_b32_e32 v158, 6, v158
	v_cndmask_b32_e32 v158, 0, v158, vcc
	v_or_b32_e32 v158, v158, v187
	v_mov_b32_e32 v159, v65
	v_lshl_add_u64 v[160:161], v[158:159], 2, s[12:13]
	global_load_dwordx4 v[216:219], v[160:161], off offset:16
	global_load_dwordx4 v[212:215], v[160:161], off
	v_add_u32_e32 v158, 16, v189
	v_cmp_lt_i32_e32 vcc, s3, v158
	v_add_u32_e32 v159, 0xffffbf00, v158
	s_nop 1
	v_cndmask_b32_e32 v158, v158, v159, vcc
	v_add_u32_e32 v159, 0xffffff00, v158
	v_cmp_lt_i32_e32 vcc, s17, v158
	v_lshrrev_b32_e32 v159, 6, v159
	v_and_b32_e32 v158, 63, v158
	v_cndmask_b32_e64 v158, v158, v159, s[4:5]
	v_lshlrev_b32_e32 v158, 6, v158
	v_cndmask_b32_e32 v158, 0, v158, vcc
	v_or_b32_e32 v158, v158, v187
	v_mov_b32_e32 v159, v65
	v_lshl_add_u64 v[160:161], v[158:159], 2, s[12:13]
	global_load_dwordx4 v[224:227], v[160:161], off offset:16
	global_load_dwordx4 v[220:223], v[160:161], off
	v_add_u32_e32 v158, 32, v189
	v_cmp_lt_i32_e32 vcc, s3, v158
	v_add_u32_e32 v159, 0xffffbf00, v158
	s_nop 1
	v_cndmask_b32_e32 v158, v158, v159, vcc
	v_add_u32_e32 v159, 0xffffff00, v158
	v_cmp_lt_i32_e32 vcc, s17, v158
	v_lshrrev_b32_e32 v159, 6, v159
	v_and_b32_e32 v158, 63, v158
	v_cndmask_b32_e64 v158, v158, v159, s[4:5]
	v_lshlrev_b32_e32 v158, 6, v158
	v_cndmask_b32_e32 v158, 0, v158, vcc
	v_or_b32_e32 v158, v158, v187
	v_mov_b32_e32 v159, v65
	v_lshl_add_u64 v[160:161], v[158:159], 2, s[12:13]
	global_load_dwordx4 v[232:235], v[160:161], off offset:16
	global_load_dwordx4 v[228:231], v[160:161], off
	v_add_u32_e32 v158, 48, v189
	v_cmp_lt_i32_e32 vcc, s3, v158
	v_add_u32_e32 v159, 0xffffbf00, v158
	s_nop 1
	v_cndmask_b32_e32 v158, v158, v159, vcc
	v_add_u32_e32 v159, 0xffffff00, v158
	v_cmp_lt_i32_e32 vcc, s17, v158
	v_lshrrev_b32_e32 v159, 6, v159
	v_and_b32_e32 v158, 63, v158
	v_cndmask_b32_e64 v158, v158, v159, s[4:5]
	v_lshlrev_b32_e32 v158, 6, v158
	v_cndmask_b32_e32 v158, 0, v158, vcc
	v_or_b32_e32 v158, v158, v187
	v_mov_b32_e32 v159, v65
	v_lshl_add_u64 v[160:161], v[158:159], 2, s[12:13]
	global_load_dwordx4 v[180:183], v[160:161], off offset:16
	global_load_dwordx4 v[176:179], v[160:161], off
	s_waitcnt vmcnt(6)
	v_mov_b32_e32 v158, v189
	v_mad_i64_i32 v[236:237], s[24:25], v158, s19, v[136:137]
	v_lshl_add_u64 v[236:237], v[236:237], 0, v[138:139]
	v_pk_mul_f32 v[164:165], v[134:135], v[126:127] op_sel_hi:[0,1]
	v_pk_mul_f32 v[166:167], v[134:135], v[128:129] op_sel_hi:[0,1]
	v_pk_mul_f32 v[168:169], v[134:135], v[122:123] op_sel_hi:[0,1]
	v_pk_mul_f32 v[170:171], v[134:135], v[124:125] op_sel_hi:[0,1]
	v_pk_mul_f32 v[172:173], v[164:165], v[212:213]
	v_pk_mul_f32 v[174:175], v[164:165], v[212:213] op_sel:[0,1] op_sel_hi:[1,0]
	v_sub_f32_e32 v140, v172, v173
	v_add_f32_e32 v141, v174, v175
	v_pk_mul_f32 v[172:173], v[166:167], v[214:215]
	v_pk_mul_f32 v[174:175], v[166:167], v[214:215] op_sel:[0,1] op_sel_hi:[1,0]
	v_sub_f32_e32 v142, v172, v173
	v_add_f32_e32 v143, v174, v175
	v_pk_mul_f32 v[172:173], v[168:169], v[216:217]
	v_pk_mul_f32 v[174:175], v[168:169], v[216:217] op_sel:[0,1] op_sel_hi:[1,0]
	v_sub_f32_e32 v144, v172, v173
	v_add_f32_e32 v145, v174, v175
	v_pk_mul_f32 v[172:173], v[170:171], v[218:219]
	v_pk_mul_f32 v[174:175], v[170:171], v[218:219] op_sel:[0,1] op_sel_hi:[1,0]
	v_sub_f32_e32 v190, v172, v173
	v_add_f32_e32 v191, v174, v175
	v_cvt_pk_bf16_f32 v192, v140, v141
	v_cvt_pk_bf16_f32 v193, v142, v143
	v_cvt_pk_bf16_f32 v194, v144, v145
	v_cvt_pk_bf16_f32 v195, v190, v191
	global_store_dwordx4 v[236:237], v[192:195], off
	s_nop 1
	v_pk_mul_f32 v[164:165], v[134:135], v[114:115] op_sel_hi:[0,1]
	v_pk_mul_f32 v[166:167], v[134:135], v[116:117] op_sel_hi:[0,1]
	v_pk_mul_f32 v[168:169], v[134:135], v[106:107] op_sel_hi:[0,1]
	v_pk_mul_f32 v[170:171], v[134:135], v[108:109] op_sel_hi:[0,1]
	v_pk_mul_f32 v[172:173], v[164:165], v[212:213]
	v_pk_mul_f32 v[174:175], v[164:165], v[212:213] op_sel:[0,1] op_sel_hi:[1,0]
	v_sub_f32_e32 v140, v172, v173
	v_add_f32_e32 v141, v174, v175
	v_pk_mul_f32 v[172:173], v[166:167], v[214:215]
	v_pk_mul_f32 v[174:175], v[166:167], v[214:215] op_sel:[0,1] op_sel_hi:[1,0]
	v_sub_f32_e32 v142, v172, v173
	v_add_f32_e32 v143, v174, v175
	v_pk_mul_f32 v[172:173], v[168:169], v[216:217]
	v_pk_mul_f32 v[174:175], v[168:169], v[216:217] op_sel:[0,1] op_sel_hi:[1,0]
	v_sub_f32_e32 v144, v172, v173
	v_add_f32_e32 v145, v174, v175
	v_pk_mul_f32 v[172:173], v[170:171], v[218:219]
	v_pk_mul_f32 v[174:175], v[170:171], v[218:219] op_sel:[0,1] op_sel_hi:[1,0]
	v_sub_f32_e32 v190, v172, v173
	v_add_f32_e32 v191, v174, v175
	v_cvt_pk_bf16_f32 v192, v140, v141
	v_cvt_pk_bf16_f32 v193, v142, v143
	v_cvt_pk_bf16_f32 v194, v144, v145
	v_cvt_pk_bf16_f32 v195, v190, v191
	global_store_dwordx4 v[236:237], v[192:195], off offset:256
	s_nop 1
	v_add_u32_e32 v158, 128, v189
	v_cmp_lt_i32_e32 vcc, s3, v158
	v_add_u32_e32 v159, 0xffffbf00, v158
	s_nop 1
	v_cndmask_b32_e32 v158, v158, v159, vcc
	v_add_u32_e32 v159, 0xffffff00, v158
	v_cmp_lt_i32_e32 vcc, s17, v158
	v_lshrrev_b32_e32 v159, 6, v159
	v_and_b32_e32 v158, 63, v158
	v_cndmask_b32_e64 v158, v158, v159, s[4:5]
	v_lshlrev_b32_e32 v158, 6, v158
	v_cndmask_b32_e32 v158, 0, v158, vcc
	v_or_b32_e32 v158, v158, v187
	v_mov_b32_e32 v159, v65
	v_lshl_add_u64 v[160:161], v[158:159], 2, s[12:13]
	global_load_dwordx4 v[216:219], v[160:161], off offset:16
	global_load_dwordx4 v[212:215], v[160:161], off
	s_waitcnt vmcnt(8)
	v_add_u32_e32 v158, 16, v189
	v_mad_i64_i32 v[236:237], s[24:25], v158, s19, v[136:137]
	v_lshl_add_u64 v[236:237], v[236:237], 0, v[138:139]
	v_pk_mul_f32 v[164:165], v[134:135], v[118:119] op_sel_hi:[0,1]
	v_pk_mul_f32 v[166:167], v[134:135], v[120:121] op_sel_hi:[0,1]
	v_pk_mul_f32 v[168:169], v[134:135], v[110:111] op_sel_hi:[0,1]
	v_pk_mul_f32 v[170:171], v[134:135], v[112:113] op_sel_hi:[0,1]
	v_pk_mul_f32 v[172:173], v[164:165], v[220:221]
	v_pk_mul_f32 v[174:175], v[164:165], v[220:221] op_sel:[0,1] op_sel_hi:[1,0]
	v_sub_f32_e32 v140, v172, v173
	v_add_f32_e32 v141, v174, v175
	v_pk_mul_f32 v[172:173], v[166:167], v[222:223]
	v_pk_mul_f32 v[174:175], v[166:167], v[222:223] op_sel:[0,1] op_sel_hi:[1,0]
	v_sub_f32_e32 v142, v172, v173
	v_add_f32_e32 v143, v174, v175
	v_pk_mul_f32 v[172:173], v[168:169], v[224:225]
	v_pk_mul_f32 v[174:175], v[168:169], v[224:225] op_sel:[0,1] op_sel_hi:[1,0]
	v_sub_f32_e32 v144, v172, v173
	v_add_f32_e32 v145, v174, v175
	v_pk_mul_f32 v[172:173], v[170:171], v[226:227]
	v_pk_mul_f32 v[174:175], v[170:171], v[226:227] op_sel:[0,1] op_sel_hi:[1,0]
	v_sub_f32_e32 v190, v172, v173
	v_add_f32_e32 v191, v174, v175
	v_cvt_pk_bf16_f32 v192, v140, v141
	v_cvt_pk_bf16_f32 v193, v142, v143
	v_cvt_pk_bf16_f32 v194, v144, v145
	v_cvt_pk_bf16_f32 v195, v190, v191
	global_store_dwordx4 v[236:237], v[192:195], off
	s_nop 1
	v_pk_mul_f32 v[164:165], v[134:135], v[98:99] op_sel_hi:[0,1]
	v_pk_mul_f32 v[166:167], v[134:135], v[100:101] op_sel_hi:[0,1]
	v_pk_mul_f32 v[168:169], v[134:135], v[90:91] op_sel_hi:[0,1]
	v_pk_mul_f32 v[170:171], v[134:135], v[92:93] op_sel_hi:[0,1]
	v_pk_mul_f32 v[172:173], v[164:165], v[220:221]
	v_pk_mul_f32 v[174:175], v[164:165], v[220:221] op_sel:[0,1] op_sel_hi:[1,0]
	v_sub_f32_e32 v140, v172, v173
	v_add_f32_e32 v141, v174, v175
	v_pk_mul_f32 v[172:173], v[166:167], v[222:223]
	v_pk_mul_f32 v[174:175], v[166:167], v[222:223] op_sel:[0,1] op_sel_hi:[1,0]
	v_sub_f32_e32 v142, v172, v173
	v_add_f32_e32 v143, v174, v175
	v_pk_mul_f32 v[172:173], v[168:169], v[224:225]
	v_pk_mul_f32 v[174:175], v[168:169], v[224:225] op_sel:[0,1] op_sel_hi:[1,0]
	v_sub_f32_e32 v144, v172, v173
	v_add_f32_e32 v145, v174, v175
	v_pk_mul_f32 v[172:173], v[170:171], v[226:227]
	v_pk_mul_f32 v[174:175], v[170:171], v[226:227] op_sel:[0,1] op_sel_hi:[1,0]
	v_sub_f32_e32 v190, v172, v173
	v_add_f32_e32 v191, v174, v175
	v_cvt_pk_bf16_f32 v192, v140, v141
	v_cvt_pk_bf16_f32 v193, v142, v143
	v_cvt_pk_bf16_f32 v194, v144, v145
	v_cvt_pk_bf16_f32 v195, v190, v191
	global_store_dwordx4 v[236:237], v[192:195], off offset:256
	s_nop 1
	v_add_u32_e32 v158, 144, v189
	v_cmp_lt_i32_e32 vcc, s3, v158
	v_add_u32_e32 v159, 0xffffbf00, v158
	s_nop 1
	v_cndmask_b32_e32 v158, v158, v159, vcc
	v_add_u32_e32 v159, 0xffffff00, v158
	v_cmp_lt_i32_e32 vcc, s17, v158
	v_lshrrev_b32_e32 v159, 6, v159
	v_and_b32_e32 v158, 63, v158
	v_cndmask_b32_e64 v158, v158, v159, s[4:5]
	v_lshlrev_b32_e32 v158, 6, v158
	v_cndmask_b32_e32 v158, 0, v158, vcc
	v_or_b32_e32 v158, v158, v187
	v_mov_b32_e32 v159, v65
	v_lshl_add_u64 v[160:161], v[158:159], 2, s[12:13]
	global_load_dwordx4 v[224:227], v[160:161], off offset:16
	global_load_dwordx4 v[220:223], v[160:161], off
	s_waitcnt vmcnt(10)
	v_add_u32_e32 v158, 32, v189
	v_mad_i64_i32 v[236:237], s[24:25], v158, s19, v[136:137]
	v_lshl_add_u64 v[236:237], v[236:237], 0, v[138:139]
	v_pk_mul_f32 v[164:165], v[134:135], v[102:103] op_sel_hi:[0,1]
	v_pk_mul_f32 v[166:167], v[134:135], v[104:105] op_sel_hi:[0,1]
	v_pk_mul_f32 v[168:169], v[134:135], v[94:95] op_sel_hi:[0,1]
	v_pk_mul_f32 v[170:171], v[134:135], v[96:97] op_sel_hi:[0,1]
	v_pk_mul_f32 v[172:173], v[164:165], v[228:229]
	v_pk_mul_f32 v[174:175], v[164:165], v[228:229] op_sel:[0,1] op_sel_hi:[1,0]
	v_sub_f32_e32 v140, v172, v173
	v_add_f32_e32 v141, v174, v175
	v_pk_mul_f32 v[172:173], v[166:167], v[230:231]
	v_pk_mul_f32 v[174:175], v[166:167], v[230:231] op_sel:[0,1] op_sel_hi:[1,0]
	v_sub_f32_e32 v142, v172, v173
	v_add_f32_e32 v143, v174, v175
	v_pk_mul_f32 v[172:173], v[168:169], v[232:233]
	v_pk_mul_f32 v[174:175], v[168:169], v[232:233] op_sel:[0,1] op_sel_hi:[1,0]
	v_sub_f32_e32 v144, v172, v173
	v_add_f32_e32 v145, v174, v175
	v_pk_mul_f32 v[172:173], v[170:171], v[234:235]
	v_pk_mul_f32 v[174:175], v[170:171], v[234:235] op_sel:[0,1] op_sel_hi:[1,0]
	v_sub_f32_e32 v190, v172, v173
	v_add_f32_e32 v191, v174, v175
	v_cvt_pk_bf16_f32 v192, v140, v141
	v_cvt_pk_bf16_f32 v193, v142, v143
	v_cvt_pk_bf16_f32 v194, v144, v145
	v_cvt_pk_bf16_f32 v195, v190, v191
	global_store_dwordx4 v[236:237], v[192:195], off
	s_nop 1
	v_pk_mul_f32 v[164:165], v[134:135], v[82:83] op_sel_hi:[0,1]
	v_pk_mul_f32 v[166:167], v[134:135], v[84:85] op_sel_hi:[0,1]
	v_pk_mul_f32 v[168:169], v[134:135], v[74:75] op_sel_hi:[0,1]
	v_pk_mul_f32 v[170:171], v[134:135], v[76:77] op_sel_hi:[0,1]
	v_pk_mul_f32 v[172:173], v[164:165], v[228:229]
	v_pk_mul_f32 v[174:175], v[164:165], v[228:229] op_sel:[0,1] op_sel_hi:[1,0]
	v_sub_f32_e32 v140, v172, v173
	v_add_f32_e32 v141, v174, v175
	v_pk_mul_f32 v[172:173], v[166:167], v[230:231]
	v_pk_mul_f32 v[174:175], v[166:167], v[230:231] op_sel:[0,1] op_sel_hi:[1,0]
	v_sub_f32_e32 v142, v172, v173
	v_add_f32_e32 v143, v174, v175
	v_pk_mul_f32 v[172:173], v[168:169], v[232:233]
	v_pk_mul_f32 v[174:175], v[168:169], v[232:233] op_sel:[0,1] op_sel_hi:[1,0]
	v_sub_f32_e32 v144, v172, v173
	v_add_f32_e32 v145, v174, v175
	v_pk_mul_f32 v[172:173], v[170:171], v[234:235]
	v_pk_mul_f32 v[174:175], v[170:171], v[234:235] op_sel:[0,1] op_sel_hi:[1,0]
	v_sub_f32_e32 v190, v172, v173
	v_add_f32_e32 v191, v174, v175
	v_cvt_pk_bf16_f32 v192, v140, v141
	v_cvt_pk_bf16_f32 v193, v142, v143
	v_cvt_pk_bf16_f32 v194, v144, v145
	v_cvt_pk_bf16_f32 v195, v190, v191
	global_store_dwordx4 v[236:237], v[192:195], off offset:256
	s_nop 1
	v_add_u32_e32 v158, 160, v189
	v_cmp_lt_i32_e32 vcc, s3, v158
	v_add_u32_e32 v159, 0xffffbf00, v158
	s_nop 1
	v_cndmask_b32_e32 v158, v158, v159, vcc
	v_add_u32_e32 v159, 0xffffff00, v158
	v_cmp_lt_i32_e32 vcc, s17, v158
	v_lshrrev_b32_e32 v159, 6, v159
	v_and_b32_e32 v158, 63, v158
	v_cndmask_b32_e64 v158, v158, v159, s[4:5]
	v_lshlrev_b32_e32 v158, 6, v158
	v_cndmask_b32_e32 v158, 0, v158, vcc
	v_or_b32_e32 v158, v158, v187
	v_mov_b32_e32 v159, v65
	v_lshl_add_u64 v[160:161], v[158:159], 2, s[12:13]
	global_load_dwordx4 v[232:235], v[160:161], off offset:16
	global_load_dwordx4 v[228:231], v[160:161], off
	s_waitcnt vmcnt(12)
	v_add_u32_e32 v158, 48, v189
	v_mad_i64_i32 v[236:237], s[24:25], v158, s19, v[136:137]
	v_lshl_add_u64 v[236:237], v[236:237], 0, v[138:139]
	v_pk_mul_f32 v[164:165], v[134:135], v[86:87] op_sel_hi:[0,1]
	v_pk_mul_f32 v[166:167], v[134:135], v[88:89] op_sel_hi:[0,1]
	v_pk_mul_f32 v[168:169], v[134:135], v[78:79] op_sel_hi:[0,1]
	v_pk_mul_f32 v[170:171], v[134:135], v[80:81] op_sel_hi:[0,1]
	v_pk_mul_f32 v[172:173], v[164:165], v[176:177]
	v_pk_mul_f32 v[174:175], v[164:165], v[176:177] op_sel:[0,1] op_sel_hi:[1,0]
	v_sub_f32_e32 v140, v172, v173
	v_add_f32_e32 v141, v174, v175
	v_pk_mul_f32 v[172:173], v[166:167], v[178:179]
	v_pk_mul_f32 v[174:175], v[166:167], v[178:179] op_sel:[0,1] op_sel_hi:[1,0]
	v_sub_f32_e32 v142, v172, v173
	v_add_f32_e32 v143, v174, v175
	v_pk_mul_f32 v[172:173], v[168:169], v[180:181]
	v_pk_mul_f32 v[174:175], v[168:169], v[180:181] op_sel:[0,1] op_sel_hi:[1,0]
	v_sub_f32_e32 v144, v172, v173
	v_add_f32_e32 v145, v174, v175
	v_pk_mul_f32 v[172:173], v[170:171], v[182:183]
	v_pk_mul_f32 v[174:175], v[170:171], v[182:183] op_sel:[0,1] op_sel_hi:[1,0]
	v_sub_f32_e32 v190, v172, v173
	v_add_f32_e32 v191, v174, v175
	v_cvt_pk_bf16_f32 v192, v140, v141
	v_cvt_pk_bf16_f32 v193, v142, v143
	v_cvt_pk_bf16_f32 v194, v144, v145
	v_cvt_pk_bf16_f32 v195, v190, v191
	global_store_dwordx4 v[236:237], v[192:195], off
	s_nop 1
	v_pk_mul_f32 v[164:165], v[134:135], v[70:71] op_sel_hi:[0,1]
	v_pk_mul_f32 v[166:167], v[134:135], v[72:73] op_sel_hi:[0,1]
	v_pk_mul_f32 v[168:169], v[134:135], v[66:67] op_sel_hi:[0,1]
	v_pk_mul_f32 v[170:171], v[134:135], v[68:69] op_sel_hi:[0,1]
	v_pk_mul_f32 v[172:173], v[164:165], v[176:177]
	v_pk_mul_f32 v[174:175], v[164:165], v[176:177] op_sel:[0,1] op_sel_hi:[1,0]
	v_sub_f32_e32 v140, v172, v173
	v_add_f32_e32 v141, v174, v175
	v_pk_mul_f32 v[172:173], v[166:167], v[178:179]
	v_pk_mul_f32 v[174:175], v[166:167], v[178:179] op_sel:[0,1] op_sel_hi:[1,0]
	v_sub_f32_e32 v142, v172, v173
	v_add_f32_e32 v143, v174, v175
	v_pk_mul_f32 v[172:173], v[168:169], v[180:181]
	v_pk_mul_f32 v[174:175], v[168:169], v[180:181] op_sel:[0,1] op_sel_hi:[1,0]
	v_sub_f32_e32 v144, v172, v173
	v_add_f32_e32 v145, v174, v175
	v_pk_mul_f32 v[172:173], v[170:171], v[182:183]
	v_pk_mul_f32 v[174:175], v[170:171], v[182:183] op_sel:[0,1] op_sel_hi:[1,0]
	v_sub_f32_e32 v190, v172, v173
	v_add_f32_e32 v191, v174, v175
	v_cvt_pk_bf16_f32 v192, v140, v141
	v_cvt_pk_bf16_f32 v193, v142, v143
	v_cvt_pk_bf16_f32 v194, v144, v145
	v_cvt_pk_bf16_f32 v195, v190, v191
	global_store_dwordx4 v[236:237], v[192:195], off offset:256
	s_nop 1
	v_add_u32_e32 v158, 176, v189
	v_cmp_lt_i32_e32 vcc, s3, v158
	v_add_u32_e32 v159, 0xffffbf00, v158
	s_nop 1
	v_cndmask_b32_e32 v158, v158, v159, vcc
	v_add_u32_e32 v159, 0xffffff00, v158
	v_cmp_lt_i32_e32 vcc, s17, v158
	v_lshrrev_b32_e32 v159, 6, v159
	v_and_b32_e32 v158, 63, v158
	v_cndmask_b32_e64 v158, v158, v159, s[4:5]
	v_lshlrev_b32_e32 v158, 6, v158
	v_cndmask_b32_e32 v158, 0, v158, vcc
	v_or_b32_e32 v158, v158, v187
	v_mov_b32_e32 v159, v65
	v_lshl_add_u64 v[160:161], v[158:159], 2, s[12:13]
	global_load_dwordx4 v[180:183], v[160:161], off offset:16
	global_load_dwordx4 v[176:179], v[160:161], off
	s_waitcnt vmcnt(12)
	v_add_u32_e32 v158, 128, v189
	v_mad_i64_i32 v[236:237], s[24:25], v158, s19, v[136:137]
	v_lshl_add_u64 v[236:237], v[236:237], 0, v[138:139]
	v_pk_mul_f32 v[164:165], v[134:135], v[60:61] op_sel_hi:[0,1]
	v_pk_mul_f32 v[166:167], v[134:135], v[62:63] op_sel_hi:[0,1]
	v_pk_mul_f32 v[168:169], v[134:135], v[56:57] op_sel_hi:[0,1]
	v_pk_mul_f32 v[170:171], v[134:135], v[58:59] op_sel_hi:[0,1]
	v_pk_mul_f32 v[172:173], v[164:165], v[212:213]
	v_pk_mul_f32 v[174:175], v[164:165], v[212:213] op_sel:[0,1] op_sel_hi:[1,0]
	v_sub_f32_e32 v140, v172, v173
	v_add_f32_e32 v141, v174, v175
	v_pk_mul_f32 v[172:173], v[166:167], v[214:215]
	v_pk_mul_f32 v[174:175], v[166:167], v[214:215] op_sel:[0,1] op_sel_hi:[1,0]
	v_sub_f32_e32 v142, v172, v173
	v_add_f32_e32 v143, v174, v175
	v_pk_mul_f32 v[172:173], v[168:169], v[216:217]
	v_pk_mul_f32 v[174:175], v[168:169], v[216:217] op_sel:[0,1] op_sel_hi:[1,0]
	v_sub_f32_e32 v144, v172, v173
	v_add_f32_e32 v145, v174, v175
	v_pk_mul_f32 v[172:173], v[170:171], v[218:219]
	v_pk_mul_f32 v[174:175], v[170:171], v[218:219] op_sel:[0,1] op_sel_hi:[1,0]
	v_sub_f32_e32 v190, v172, v173
	v_add_f32_e32 v191, v174, v175
	v_cvt_pk_bf16_f32 v192, v140, v141
	v_cvt_pk_bf16_f32 v193, v142, v143
	v_cvt_pk_bf16_f32 v194, v144, v145
	v_cvt_pk_bf16_f32 v195, v190, v191
	global_store_dwordx4 v[236:237], v[192:195], off
	s_nop 1
	v_pk_mul_f32 v[164:165], v[134:135], v[48:49] op_sel_hi:[0,1]
	v_pk_mul_f32 v[166:167], v[134:135], v[50:51] op_sel_hi:[0,1]
	v_pk_mul_f32 v[168:169], v[134:135], v[40:41] op_sel_hi:[0,1]
	v_pk_mul_f32 v[170:171], v[134:135], v[42:43] op_sel_hi:[0,1]
	v_pk_mul_f32 v[172:173], v[164:165], v[212:213]
	v_pk_mul_f32 v[174:175], v[164:165], v[212:213] op_sel:[0,1] op_sel_hi:[1,0]
	v_sub_f32_e32 v140, v172, v173
	v_add_f32_e32 v141, v174, v175
	v_pk_mul_f32 v[172:173], v[166:167], v[214:215]
	v_pk_mul_f32 v[174:175], v[166:167], v[214:215] op_sel:[0,1] op_sel_hi:[1,0]
	v_sub_f32_e32 v142, v172, v173
	v_add_f32_e32 v143, v174, v175
	v_pk_mul_f32 v[172:173], v[168:169], v[216:217]
	v_pk_mul_f32 v[174:175], v[168:169], v[216:217] op_sel:[0,1] op_sel_hi:[1,0]
	v_sub_f32_e32 v144, v172, v173
	v_add_f32_e32 v145, v174, v175
	v_pk_mul_f32 v[172:173], v[170:171], v[218:219]
	v_pk_mul_f32 v[174:175], v[170:171], v[218:219] op_sel:[0,1] op_sel_hi:[1,0]
	v_sub_f32_e32 v190, v172, v173
	v_add_f32_e32 v191, v174, v175
	v_cvt_pk_bf16_f32 v192, v140, v141
	v_cvt_pk_bf16_f32 v193, v142, v143
	v_cvt_pk_bf16_f32 v194, v144, v145
	v_cvt_pk_bf16_f32 v195, v190, v191
	global_store_dwordx4 v[236:237], v[192:195], off offset:256
	s_nop 1
	s_waitcnt vmcnt(10)
	v_add_u32_e32 v158, 144, v189
	v_mad_i64_i32 v[236:237], s[24:25], v158, s19, v[136:137]
	v_lshl_add_u64 v[236:237], v[236:237], 0, v[138:139]
	v_pk_mul_f32 v[164:165], v[134:135], v[52:53] op_sel_hi:[0,1]
	v_pk_mul_f32 v[166:167], v[134:135], v[54:55] op_sel_hi:[0,1]
	v_pk_mul_f32 v[168:169], v[134:135], v[44:45] op_sel_hi:[0,1]
	v_pk_mul_f32 v[170:171], v[134:135], v[46:47] op_sel_hi:[0,1]
	v_pk_mul_f32 v[172:173], v[164:165], v[220:221]
	v_pk_mul_f32 v[174:175], v[164:165], v[220:221] op_sel:[0,1] op_sel_hi:[1,0]
	v_sub_f32_e32 v140, v172, v173
	v_add_f32_e32 v141, v174, v175
	v_pk_mul_f32 v[172:173], v[166:167], v[222:223]
	v_pk_mul_f32 v[174:175], v[166:167], v[222:223] op_sel:[0,1] op_sel_hi:[1,0]
	v_sub_f32_e32 v142, v172, v173
	v_add_f32_e32 v143, v174, v175
	v_pk_mul_f32 v[172:173], v[168:169], v[224:225]
	v_pk_mul_f32 v[174:175], v[168:169], v[224:225] op_sel:[0,1] op_sel_hi:[1,0]
	v_sub_f32_e32 v144, v172, v173
	v_add_f32_e32 v145, v174, v175
	v_pk_mul_f32 v[172:173], v[170:171], v[226:227]
	v_pk_mul_f32 v[174:175], v[170:171], v[226:227] op_sel:[0,1] op_sel_hi:[1,0]
	v_sub_f32_e32 v190, v172, v173
	v_add_f32_e32 v191, v174, v175
	v_cvt_pk_bf16_f32 v192, v140, v141
	v_cvt_pk_bf16_f32 v193, v142, v143
	v_cvt_pk_bf16_f32 v194, v144, v145
	v_cvt_pk_bf16_f32 v195, v190, v191
	global_store_dwordx4 v[236:237], v[192:195], off
	s_nop 1
	v_pk_mul_f32 v[164:165], v[134:135], v[32:33] op_sel_hi:[0,1]
	v_pk_mul_f32 v[166:167], v[134:135], v[34:35] op_sel_hi:[0,1]
	v_pk_mul_f32 v[168:169], v[134:135], v[24:25] op_sel_hi:[0,1]
	v_pk_mul_f32 v[170:171], v[134:135], v[26:27] op_sel_hi:[0,1]
	v_pk_mul_f32 v[172:173], v[164:165], v[220:221]
	v_pk_mul_f32 v[174:175], v[164:165], v[220:221] op_sel:[0,1] op_sel_hi:[1,0]
	v_sub_f32_e32 v140, v172, v173
	v_add_f32_e32 v141, v174, v175
	v_pk_mul_f32 v[172:173], v[166:167], v[222:223]
	v_pk_mul_f32 v[174:175], v[166:167], v[222:223] op_sel:[0,1] op_sel_hi:[1,0]
	v_sub_f32_e32 v142, v172, v173
	v_add_f32_e32 v143, v174, v175
	v_pk_mul_f32 v[172:173], v[168:169], v[224:225]
	v_pk_mul_f32 v[174:175], v[168:169], v[224:225] op_sel:[0,1] op_sel_hi:[1,0]
	v_sub_f32_e32 v144, v172, v173
	v_add_f32_e32 v145, v174, v175
	v_pk_mul_f32 v[172:173], v[170:171], v[226:227]
	v_pk_mul_f32 v[174:175], v[170:171], v[226:227] op_sel:[0,1] op_sel_hi:[1,0]
	v_sub_f32_e32 v190, v172, v173
	v_add_f32_e32 v191, v174, v175
	v_cvt_pk_bf16_f32 v192, v140, v141
	v_cvt_pk_bf16_f32 v193, v142, v143
	v_cvt_pk_bf16_f32 v194, v144, v145
	v_cvt_pk_bf16_f32 v195, v190, v191
	global_store_dwordx4 v[236:237], v[192:195], off offset:256
	s_nop 1
	s_waitcnt vmcnt(8)
	v_add_u32_e32 v158, 160, v189
	v_mad_i64_i32 v[236:237], s[24:25], v158, s19, v[136:137]
	v_lshl_add_u64 v[236:237], v[236:237], 0, v[138:139]
	v_pk_mul_f32 v[164:165], v[134:135], v[36:37] op_sel_hi:[0,1]
	v_pk_mul_f32 v[166:167], v[134:135], v[38:39] op_sel_hi:[0,1]
	v_pk_mul_f32 v[168:169], v[134:135], v[28:29] op_sel_hi:[0,1]
	v_pk_mul_f32 v[170:171], v[134:135], v[30:31] op_sel_hi:[0,1]
	v_pk_mul_f32 v[172:173], v[164:165], v[228:229]
	v_pk_mul_f32 v[174:175], v[164:165], v[228:229] op_sel:[0,1] op_sel_hi:[1,0]
	v_sub_f32_e32 v140, v172, v173
	v_add_f32_e32 v141, v174, v175
	v_pk_mul_f32 v[172:173], v[166:167], v[230:231]
	v_pk_mul_f32 v[174:175], v[166:167], v[230:231] op_sel:[0,1] op_sel_hi:[1,0]
	v_sub_f32_e32 v142, v172, v173
	v_add_f32_e32 v143, v174, v175
	v_pk_mul_f32 v[172:173], v[168:169], v[232:233]
	v_pk_mul_f32 v[174:175], v[168:169], v[232:233] op_sel:[0,1] op_sel_hi:[1,0]
	v_sub_f32_e32 v144, v172, v173
	v_add_f32_e32 v145, v174, v175
	v_pk_mul_f32 v[172:173], v[170:171], v[234:235]
	v_pk_mul_f32 v[174:175], v[170:171], v[234:235] op_sel:[0,1] op_sel_hi:[1,0]
	v_sub_f32_e32 v190, v172, v173
	v_add_f32_e32 v191, v174, v175
	v_cvt_pk_bf16_f32 v192, v140, v141
	v_cvt_pk_bf16_f32 v193, v142, v143
	v_cvt_pk_bf16_f32 v194, v144, v145
	v_cvt_pk_bf16_f32 v195, v190, v191
	global_store_dwordx4 v[236:237], v[192:195], off
	s_nop 1
	v_pk_mul_f32 v[164:165], v[134:135], v[16:17] op_sel_hi:[0,1]
	v_pk_mul_f32 v[166:167], v[134:135], v[18:19] op_sel_hi:[0,1]
	v_pk_mul_f32 v[168:169], v[134:135], v[8:9] op_sel_hi:[0,1]
	v_pk_mul_f32 v[170:171], v[134:135], v[10:11] op_sel_hi:[0,1]
	v_pk_mul_f32 v[172:173], v[164:165], v[228:229]
	v_pk_mul_f32 v[174:175], v[164:165], v[228:229] op_sel:[0,1] op_sel_hi:[1,0]
	v_sub_f32_e32 v140, v172, v173
	v_add_f32_e32 v141, v174, v175
	v_pk_mul_f32 v[172:173], v[166:167], v[230:231]
	v_pk_mul_f32 v[174:175], v[166:167], v[230:231] op_sel:[0,1] op_sel_hi:[1,0]
	v_sub_f32_e32 v142, v172, v173
	v_add_f32_e32 v143, v174, v175
	v_pk_mul_f32 v[172:173], v[168:169], v[232:233]
	v_pk_mul_f32 v[174:175], v[168:169], v[232:233] op_sel:[0,1] op_sel_hi:[1,0]
	v_sub_f32_e32 v144, v172, v173
	v_add_f32_e32 v145, v174, v175
	v_pk_mul_f32 v[172:173], v[170:171], v[234:235]
	v_pk_mul_f32 v[174:175], v[170:171], v[234:235] op_sel:[0,1] op_sel_hi:[1,0]
	v_sub_f32_e32 v190, v172, v173
	v_add_f32_e32 v191, v174, v175
	v_cvt_pk_bf16_f32 v192, v140, v141
	v_cvt_pk_bf16_f32 v193, v142, v143
	v_cvt_pk_bf16_f32 v194, v144, v145
	v_cvt_pk_bf16_f32 v195, v190, v191
	global_store_dwordx4 v[236:237], v[192:195], off offset:256
	s_nop 1
	s_waitcnt vmcnt(6)
	v_add_u32_e32 v158, 176, v189
	v_mad_i64_i32 v[162:163], s[24:25], v158, s19, v[136:137]
	v_lshl_add_u64 v[162:163], v[162:163], 0, v[138:139]
	v_pk_mul_f32 v[164:165], v[134:135], v[20:21] op_sel_hi:[0,1]
	v_pk_mul_f32 v[166:167], v[134:135], v[22:23] op_sel_hi:[0,1]
	v_pk_mul_f32 v[168:169], v[134:135], v[12:13] op_sel_hi:[0,1]
	v_pk_mul_f32 v[170:171], v[134:135], v[14:15] op_sel_hi:[0,1]
	v_pk_mul_f32 v[172:173], v[164:165], v[176:177]
	v_pk_mul_f32 v[174:175], v[164:165], v[176:177] op_sel:[0,1] op_sel_hi:[1,0]
	v_sub_f32_e32 v140, v172, v173
	v_add_f32_e32 v141, v174, v175
	v_pk_mul_f32 v[172:173], v[166:167], v[178:179]
	v_pk_mul_f32 v[174:175], v[166:167], v[178:179] op_sel:[0,1] op_sel_hi:[1,0]
	v_sub_f32_e32 v142, v172, v173
	v_add_f32_e32 v143, v174, v175
	v_pk_mul_f32 v[172:173], v[168:169], v[180:181]
	v_pk_mul_f32 v[174:175], v[168:169], v[180:181] op_sel:[0,1] op_sel_hi:[1,0]
	v_sub_f32_e32 v144, v172, v173
	v_add_f32_e32 v145, v174, v175
	v_pk_mul_f32 v[172:173], v[170:171], v[182:183]
	v_pk_mul_f32 v[174:175], v[170:171], v[182:183] op_sel:[0,1] op_sel_hi:[1,0]
	v_sub_f32_e32 v190, v172, v173
	v_add_f32_e32 v191, v174, v175
	v_cvt_pk_bf16_f32 v192, v140, v141
	v_cvt_pk_bf16_f32 v193, v142, v143
	v_cvt_pk_bf16_f32 v194, v144, v145
	v_cvt_pk_bf16_f32 v195, v190, v191
	global_store_dwordx4 v[162:163], v[192:195], off
	s_nop 1
	v_pk_mul_f32 v[164:165], v[134:135], v[4:5] op_sel_hi:[0,1]
	v_pk_mul_f32 v[166:167], v[134:135], v[6:7] op_sel_hi:[0,1]
	v_pk_mul_f32 v[168:169], v[134:135], v[0:1] op_sel_hi:[0,1]
	v_pk_mul_f32 v[170:171], v[134:135], v[2:3] op_sel_hi:[0,1]
	v_pk_mul_f32 v[172:173], v[164:165], v[176:177]
	v_pk_mul_f32 v[174:175], v[164:165], v[176:177] op_sel:[0,1] op_sel_hi:[1,0]
	v_sub_f32_e32 v140, v172, v173
	v_add_f32_e32 v141, v174, v175
	v_pk_mul_f32 v[172:173], v[166:167], v[178:179]
	v_pk_mul_f32 v[174:175], v[166:167], v[178:179] op_sel:[0,1] op_sel_hi:[1,0]
	v_sub_f32_e32 v142, v172, v173
	v_add_f32_e32 v143, v174, v175
	v_pk_mul_f32 v[172:173], v[168:169], v[180:181]
	v_pk_mul_f32 v[174:175], v[168:169], v[180:181] op_sel:[0,1] op_sel_hi:[1,0]
	v_sub_f32_e32 v144, v172, v173
	v_add_f32_e32 v145, v174, v175
	v_pk_mul_f32 v[172:173], v[170:171], v[182:183]
	v_pk_mul_f32 v[174:175], v[170:171], v[182:183] op_sel:[0,1] op_sel_hi:[1,0]
	v_sub_f32_e32 v190, v172, v173
	v_add_f32_e32 v191, v174, v175
	v_cvt_pk_bf16_f32 v130, v140, v141
	v_cvt_pk_bf16_f32 v131, v142, v143
	v_cvt_pk_bf16_f32 v132, v144, v145
	v_cvt_pk_bf16_f32 v133, v190, v191
	s_branch .LBB0_325
